# out-proj epilogue, layer-0 path: the four f32 residual loads of each row group issued together (one wait per group instead of one per load)
# speedup vs baseline: 1.0037x; 1.0037x over previous
; __device__ __forceinline__ unsigned cvt_pk_bf16(float lo, float hi) { unsigned r; asm volatile("v_cvt_pk_bf16_f32 %0, %1, %2" : "=v"(r) : "v"(lo), "v"(hi)); return r; }
;     __device__ __forceinline__ void operator()(const f32x4 (&acc)[2][2][4][2], const Unit& u, int wr, int wc, int fr, int fq) const {
;         const int row0 = u.pm * BM + wr * 64 + fr, col0 = u.pn * BM + wc * 32 + 4 * fq;
; #pragma unroll
;         for (int ai = 0; ai < 2; ++ai)
; #pragma unroll
;             for (int m = 0; m < 4; ++m) { const int row = row0 + ai * HALF + m * 16; const size_t ro = (size_t)row * 2048 + col0;
;                 float s = 0.f;
; #pragma unroll
;                 for (int bj = 0; bj < 2; ++bj)
; #pragma unroll
;                     for (int n = 0; n < 2; ++n) { f32x4 r;
;                         if (R32) r = *(const f32x4*)(R32 + ro + bj * HALF + n * 16);
;                         else { typedef unsigned u32x2_t __attribute__((ext_vector_type(2))); const u32x2_t rw = *(const u32x2_t*)(R16 + ro + bj * HALF + n * 16); const unsigned r0 = rw.x, r1 = rw.y;
;                             r = (f32x4){__builtin_bit_cast(float, r0 << 16), __builtin_bit_cast(float, r0 & 0xffff0000u), __builtin_bit_cast(float, r1 << 16), __builtin_bit_cast(float, r1 & 0xffff0000u)}; }
;                         const f32x4 v = acc[ai][bj][m][n] + r;
;                         typedef unsigned u32x2_s __attribute__((ext_vector_type(2))); u32x2_s w; w.x = cvt_pk_bf16(v[0], v[1]); w.y = cvt_pk_bf16(v[2], v[3]);
;                         *(u32x2_s*)(XB + ro + bj * HALF + n * 16) = w;
.LBB0_728:
	v_and_b32_e32 v180, 15, v211
	v_lshrrev_b32_e32 v181, 4, v211
	v_lshrrev_b32_e32 v182, 3, v211
	v_bfe_u32 v183, v211, 2, 1
	v_lshrrev_b32_e32 v234, 6, v212
	v_mul_u32_u24_e32 v234, 0xc00, v234
	v_add_u32_e32 v234, 0x20400, v234
	v_mul_u32_u24_e32 v235, 0x90, v182
	v_add_u32_e32 v235, v234, v235
	v_lshl_add_u32 v235, v183, 6, v235
	v_and_b32_e32 v236, 3, v211
	v_lshl_add_u32 v235, v236, 4, v235
	v_mul_u32_u24_e32 v237, 0x90, v180
	v_add_u32_e32 v234, v234, v237
	v_lshl_add_u32 v234, v181, 3, v234
	v_sub_u32_e32 v237, v182, v180
	v_lshlrev_b32_e32 v237, 12, v237
	v_lshl_add_u32 v237, v183, 8, v237
	v_lshl_add_u32 v237, v236, 4, v237
	v_lshlrev_b32_e32 v236, 3, v181
	v_sub_u32_e32 v236, v237, v236
	v_ashrrev_i32_e32 v237, 31, v236
	v_mov_b32_e32 v206, 0x8000
	v_mov_b32_e32 v207, 0
	v_lshl_add_u32 v138, s40, 8, v152
	v_lshl_or_b32 v142, s64, 8, v154
	v_ashrrev_i32_e32 v139, 31, v138
	v_ashrrev_i32_e32 v143, 31, v142
	v_lshlrev_b64 v[128:129], 11, v[138:139]
	v_readlane_b32 s4, v252, 2
	v_lshl_add_u64 v[140:141], v[128:129], 0, v[142:143]
	v_cndmask_b32_e64 v128, 0, 1, s[88:89]
	v_readlane_b32 s5, v252, 3
	s_mov_b64 s[2:3], -1
	v_cmp_ne_u32_e64 s[40:41], 1, v128
	s_andn2_b64 vcc, exec, s[88:89]
	v_lshl_add_u64 v[144:145], v[140:141], 2, s[4:5]
	v_readlane_b32 s58, v250, 24
	v_readlane_b32 s68, v250, 25
	v_readlane_b32 s66, v250, 30
	v_readlane_b32 s6, v252, 4
	v_readlane_b32 s7, v252, 5
	v_readlane_b32 s8, v252, 6
	v_readlane_b32 s9, v252, 7
	v_readlane_b32 s10, v252, 8
	v_readlane_b32 s11, v252, 9
	v_readlane_b32 s12, v252, 10
	v_readlane_b32 s13, v252, 11
	v_readlane_b32 s14, v252, 12
	v_readlane_b32 s15, v252, 13
	v_readlane_b32 s16, v252, 14
	v_readlane_b32 s17, v252, 15
	v_readlane_b32 s18, v252, 16
	v_readlane_b32 s19, v252, 17
	s_cbranch_vccnz .LBB0_730
	global_load_dwordx4 v[156:159], v[144:145], off
	global_load_dwordx4 v[160:163], v[144:145], off offset:64
	global_load_dwordx4 v[164:167], v[144:145], off offset:512
	global_load_dwordx4 v[168:171], v[144:145], off offset:576
	s_waitcnt vmcnt(0)
	v_mov_b32_e32 v128, v156
	v_mov_b32_e32 v129, v157
	v_mov_b32_e32 v130, v158
	v_mov_b32_e32 v131, v159
	s_mov_b64 s[2:3], 0

; __device__ __forceinline__ unsigned cvt_pk_bf16(float lo, float hi) { unsigned r; asm volatile("v_cvt_pk_bf16_f32 %0, %1, %2" : "=v"(r) : "v"(lo), "v"(hi)); return r; }
;     __device__ __forceinline__ void operator()(const f32x4 (&acc)[2][2][4][2], const Unit& u, int wr, int wc, int fr, int fq) const {
;     ...
;                     for (int n = 0; n < 2; ++n) { f32x4 r;
;                         if (R32) r = *(const f32x4*)(R32 + ro + bj * HALF + n * 16);
;                         else { typedef unsigned u32x2_t __attribute__((ext_vector_type(2))); const u32x2_t rw = *(const u32x2_t*)(R16 + ro + bj * HALF + n * 16); const unsigned r0 = rw.x, r1 = rw.y;
;                             r = (f32x4){__builtin_bit_cast(float, r0 << 16), __builtin_bit_cast(float, r0 & 0xffff0000u), __builtin_bit_cast(float, r1 << 16), __builtin_bit_cast(float, r1 & 0xffff0000u)}; }
;                         const f32x4 v = acc[ai][bj][m][n] + r;
;                         typedef unsigned u32x2_s __attribute__((ext_vector_type(2))); u32x2_s w; w.x = cvt_pk_bf16(v[0], v[1]); w.y = cvt_pk_bf16(v[2], v[3]);
;                         *(u32x2_s*)(XB + ro + bj * HALF + n * 16) = w;
.LBB0_732:
	v_pk_add_f32 v[130:131], v[126:127], v[130:131]
	v_pk_add_f32 v[148:149], v[124:125], v[128:129]
	v_lshl_add_u64 v[128:129], v[140:141], 1, s[90:91]
	v_cvt_pk_bf16_f32 v124, v148, v149
	v_cvt_pk_bf16_f32 v125, v130, v131
	s_and_b64 vcc, exec, s[40:41]
	s_mov_b64 s[2:3], -1
	ds_write_b64 v234, v[124:125]
	s_cbranch_vccnz .LBB0_734
	v_mov_b32_e32 v124, v160
	v_mov_b32_e32 v125, v161
	v_mov_b32_e32 v126, v162
	v_mov_b32_e32 v127, v163
	s_mov_b64 s[2:3], 0

; __device__ __forceinline__ unsigned cvt_pk_bf16(float lo, float hi) { unsigned r; asm volatile("v_cvt_pk_bf16_f32 %0, %1, %2" : "=v"(r) : "v"(lo), "v"(hi)); return r; }
;     __device__ __forceinline__ void operator()(const f32x4 (&acc)[2][2][4][2], const Unit& u, int wr, int wc, int fr, int fq) const {
;     ...
;                     for (int n = 0; n < 2; ++n) { f32x4 r;
;                         if (R32) r = *(const f32x4*)(R32 + ro + bj * HALF + n * 16);
;                         else { typedef unsigned u32x2_t __attribute__((ext_vector_type(2))); const u32x2_t rw = *(const u32x2_t*)(R16 + ro + bj * HALF + n * 16); const unsigned r0 = rw.x, r1 = rw.y;
;                             r = (f32x4){__builtin_bit_cast(float, r0 << 16), __builtin_bit_cast(float, r0 & 0xffff0000u), __builtin_bit_cast(float, r1 << 16), __builtin_bit_cast(float, r1 & 0xffff0000u)}; }
;                         const f32x4 v = acc[ai][bj][m][n] + r;
;                         typedef unsigned u32x2_s __attribute__((ext_vector_type(2))); u32x2_s w; w.x = cvt_pk_bf16(v[0], v[1]); w.y = cvt_pk_bf16(v[2], v[3]);
;                         *(u32x2_s*)(XB + ro + bj * HALF + n * 16) = w;
.LBB0_736:
	v_pk_add_f32 v[126:127], v[122:123], v[126:127]
	v_pk_add_f32 v[124:125], v[120:121], v[124:125]
	s_and_b64 vcc, exec, s[40:41]
	v_cvt_pk_bf16_f32 v120, v124, v125
	v_cvt_pk_bf16_f32 v121, v126, v127
	s_mov_b64 s[2:3], -1
	ds_write_b64 v234, v[120:121] offset:32
	s_cbranch_vccnz .LBB0_738
	v_mov_b32_e32 v120, v164
	v_mov_b32_e32 v121, v165
	v_mov_b32_e32 v122, v166
	v_mov_b32_e32 v123, v167
	s_mov_b64 s[2:3], 0

; __device__ __forceinline__ unsigned cvt_pk_bf16(float lo, float hi) { unsigned r; asm volatile("v_cvt_pk_bf16_f32 %0, %1, %2" : "=v"(r) : "v"(lo), "v"(hi)); return r; }
;     __device__ __forceinline__ void operator()(const f32x4 (&acc)[2][2][4][2], const Unit& u, int wr, int wc, int fr, int fq) const {
;     ...
;                     for (int n = 0; n < 2; ++n) { f32x4 r;
;                         if (R32) r = *(const f32x4*)(R32 + ro + bj * HALF + n * 16);
;                         else { typedef unsigned u32x2_t __attribute__((ext_vector_type(2))); const u32x2_t rw = *(const u32x2_t*)(R16 + ro + bj * HALF + n * 16); const unsigned r0 = rw.x, r1 = rw.y;
;                             r = (f32x4){__builtin_bit_cast(float, r0 << 16), __builtin_bit_cast(float, r0 & 0xffff0000u), __builtin_bit_cast(float, r1 << 16), __builtin_bit_cast(float, r1 & 0xffff0000u)}; }
;                         const f32x4 v = acc[ai][bj][m][n] + r;
;                         typedef unsigned u32x2_s __attribute__((ext_vector_type(2))); u32x2_s w; w.x = cvt_pk_bf16(v[0], v[1]); w.y = cvt_pk_bf16(v[2], v[3]);
;                         *(u32x2_s*)(XB + ro + bj * HALF + n * 16) = w;
.LBB0_740:
	v_pk_add_f32 v[122:123], v[118:119], v[122:123]
	v_pk_add_f32 v[120:121], v[116:117], v[120:121]
	s_and_b64 vcc, exec, s[40:41]
	v_cvt_pk_bf16_f32 v116, v120, v121
	v_cvt_pk_bf16_f32 v117, v122, v123
	s_mov_b64 s[2:3], -1
	ds_write_b64 v234, v[116:117] offset:64
	s_cbranch_vccnz .LBB0_742
	v_mov_b32_e32 v116, v168
	v_mov_b32_e32 v117, v169
	v_mov_b32_e32 v118, v170
	v_mov_b32_e32 v119, v171
	s_mov_b64 s[2:3], 0

; __device__ __forceinline__ unsigned cvt_pk_bf16(float lo, float hi) { unsigned r; asm volatile("v_cvt_pk_bf16_f32 %0, %1, %2" : "=v"(r) : "v"(lo), "v"(hi)); return r; }
;     __device__ __forceinline__ void operator()(const f32x4 (&acc)[2][2][4][2], const Unit& u, int wr, int wc, int fr, int fq) const {
;     ...
;             for (int m = 0; m < 4; ++m) { const int row = row0 + ai * HALF + m * 16; const size_t ro = (size_t)row * 2048 + col0;
;                 float s = 0.f;
; #pragma unroll
;                 for (int bj = 0; bj < 2; ++bj)
; #pragma unroll
;                     for (int n = 0; n < 2; ++n) { f32x4 r;
;                         if (R32) r = *(const f32x4*)(R32 + ro + bj * HALF + n * 16);
;                         else { typedef unsigned u32x2_t __attribute__((ext_vector_type(2))); const u32x2_t rw = *(const u32x2_t*)(R16 + ro + bj * HALF + n * 16); const unsigned r0 = rw.x, r1 = rw.y;
;                             r = (f32x4){__builtin_bit_cast(float, r0 << 16), __builtin_bit_cast(float, r0 & 0xffff0000u), __builtin_bit_cast(float, r1 << 16), __builtin_bit_cast(float, r1 & 0xffff0000u)}; }
;                         const f32x4 v = acc[ai][bj][m][n] + r;
;                         typedef unsigned u32x2_s __attribute__((ext_vector_type(2))); u32x2_s w; w.x = cvt_pk_bf16(v[0], v[1]); w.y = cvt_pk_bf16(v[2], v[3]);
;                         *(u32x2_s*)(XB + ro + bj * HALF + n * 16) = w;
.LBB0_746:
	s_or_b64 exec, exec, s[2:3]
	v_or_b32_e32 v112, 16, v138
	s_waitcnt lgkmcnt(0)
	v_ashrrev_i32_e32 v113, 31, v112
	v_lshlrev_b64 v[112:113], 11, v[112:113]
	v_readlane_b32 s4, v252, 2
	v_lshl_add_u64 v[122:123], v[112:113], 0, v[142:143]
	v_readlane_b32 s5, v252, 3
	s_mov_b64 s[2:3], -1
	s_and_b64 vcc, exec, s[40:41]
	v_lshl_add_u64 v[116:117], v[122:123], 2, s[4:5]
	v_readlane_b32 s6, v252, 4
	v_readlane_b32 s7, v252, 5
	v_readlane_b32 s8, v252, 6
	v_readlane_b32 s9, v252, 7
	v_readlane_b32 s10, v252, 8
	v_readlane_b32 s11, v252, 9
	v_readlane_b32 s12, v252, 10
	v_readlane_b32 s13, v252, 11
	v_readlane_b32 s14, v252, 12
	v_readlane_b32 s15, v252, 13
	v_readlane_b32 s16, v252, 14
	v_readlane_b32 s17, v252, 15
	v_readlane_b32 s18, v252, 16
	v_readlane_b32 s19, v252, 17
	s_cbranch_vccnz .LBB0_748
	global_load_dwordx4 v[156:159], v[116:117], off
	global_load_dwordx4 v[160:163], v[116:117], off offset:64
	global_load_dwordx4 v[164:167], v[116:117], off offset:512
	global_load_dwordx4 v[168:171], v[116:117], off offset:576
	s_waitcnt vmcnt(0)
	v_mov_b32_e32 v112, v156
	v_mov_b32_e32 v113, v157
	v_mov_b32_e32 v114, v158
	v_mov_b32_e32 v115, v159
	s_mov_b64 s[2:3], 0

; __device__ __forceinline__ unsigned cvt_pk_bf16(float lo, float hi) { unsigned r; asm volatile("v_cvt_pk_bf16_f32 %0, %1, %2" : "=v"(r) : "v"(lo), "v"(hi)); return r; }
;     __device__ __forceinline__ void operator()(const f32x4 (&acc)[2][2][4][2], const Unit& u, int wr, int wc, int fr, int fq) const {
;     ...
;                     for (int n = 0; n < 2; ++n) { f32x4 r;
;                         if (R32) r = *(const f32x4*)(R32 + ro + bj * HALF + n * 16);
;                         else { typedef unsigned u32x2_t __attribute__((ext_vector_type(2))); const u32x2_t rw = *(const u32x2_t*)(R16 + ro + bj * HALF + n * 16); const unsigned r0 = rw.x, r1 = rw.y;
;                             r = (f32x4){__builtin_bit_cast(float, r0 << 16), __builtin_bit_cast(float, r0 & 0xffff0000u), __builtin_bit_cast(float, r1 << 16), __builtin_bit_cast(float, r1 & 0xffff0000u)}; }
;                         const f32x4 v = acc[ai][bj][m][n] + r;
;                         typedef unsigned u32x2_s __attribute__((ext_vector_type(2))); u32x2_s w; w.x = cvt_pk_bf16(v[0], v[1]); w.y = cvt_pk_bf16(v[2], v[3]);
;                         *(u32x2_s*)(XB + ro + bj * HALF + n * 16) = w;
.LBB0_750:
	v_pk_add_f32 v[114:115], v[110:111], v[114:115]
	v_pk_add_f32 v[120:121], v[108:109], v[112:113]
	v_lshl_add_u64 v[112:113], v[122:123], 1, s[90:91]
	v_cvt_pk_bf16_f32 v108, v120, v121
	v_cvt_pk_bf16_f32 v109, v114, v115
	s_and_b64 vcc, exec, s[40:41]
	s_mov_b64 s[2:3], -1
	ds_write_b64 v234, v[108:109]
	s_cbranch_vccnz .LBB0_752
	v_mov_b32_e32 v108, v160
	v_mov_b32_e32 v109, v161
	v_mov_b32_e32 v110, v162
	v_mov_b32_e32 v111, v163
	s_mov_b64 s[2:3], 0

; __device__ __forceinline__ unsigned cvt_pk_bf16(float lo, float hi) { unsigned r; asm volatile("v_cvt_pk_bf16_f32 %0, %1, %2" : "=v"(r) : "v"(lo), "v"(hi)); return r; }
;     __device__ __forceinline__ void operator()(const f32x4 (&acc)[2][2][4][2], const Unit& u, int wr, int wc, int fr, int fq) const {
;     ...
;                     for (int n = 0; n < 2; ++n) { f32x4 r;
;                         if (R32) r = *(const f32x4*)(R32 + ro + bj * HALF + n * 16);
;                         else { typedef unsigned u32x2_t __attribute__((ext_vector_type(2))); const u32x2_t rw = *(const u32x2_t*)(R16 + ro + bj * HALF + n * 16); const unsigned r0 = rw.x, r1 = rw.y;
;                             r = (f32x4){__builtin_bit_cast(float, r0 << 16), __builtin_bit_cast(float, r0 & 0xffff0000u), __builtin_bit_cast(float, r1 << 16), __builtin_bit_cast(float, r1 & 0xffff0000u)}; }
;                         const f32x4 v = acc[ai][bj][m][n] + r;
;                         typedef unsigned u32x2_s __attribute__((ext_vector_type(2))); u32x2_s w; w.x = cvt_pk_bf16(v[0], v[1]); w.y = cvt_pk_bf16(v[2], v[3]);
;                         *(u32x2_s*)(XB + ro + bj * HALF + n * 16) = w;
.LBB0_754:
	v_pk_add_f32 v[110:111], v[106:107], v[110:111]
	v_pk_add_f32 v[108:109], v[104:105], v[108:109]
	s_and_b64 vcc, exec, s[40:41]
	v_cvt_pk_bf16_f32 v104, v108, v109
	v_cvt_pk_bf16_f32 v105, v110, v111
	s_mov_b64 s[2:3], -1
	ds_write_b64 v234, v[104:105] offset:32
	s_cbranch_vccnz .LBB0_756
	v_mov_b32_e32 v104, v164
	v_mov_b32_e32 v105, v165
	v_mov_b32_e32 v106, v166
	v_mov_b32_e32 v107, v167
	s_mov_b64 s[2:3], 0

; __device__ __forceinline__ unsigned cvt_pk_bf16(float lo, float hi) { unsigned r; asm volatile("v_cvt_pk_bf16_f32 %0, %1, %2" : "=v"(r) : "v"(lo), "v"(hi)); return r; }
;     __device__ __forceinline__ void operator()(const f32x4 (&acc)[2][2][4][2], const Unit& u, int wr, int wc, int fr, int fq) const {
;     ...
;                     for (int n = 0; n < 2; ++n) { f32x4 r;
;                         if (R32) r = *(const f32x4*)(R32 + ro + bj * HALF + n * 16);
;                         else { typedef unsigned u32x2_t __attribute__((ext_vector_type(2))); const u32x2_t rw = *(const u32x2_t*)(R16 + ro + bj * HALF + n * 16); const unsigned r0 = rw.x, r1 = rw.y;
;                             r = (f32x4){__builtin_bit_cast(float, r0 << 16), __builtin_bit_cast(float, r0 & 0xffff0000u), __builtin_bit_cast(float, r1 << 16), __builtin_bit_cast(float, r1 & 0xffff0000u)}; }
;                         const f32x4 v = acc[ai][bj][m][n] + r;
;                         typedef unsigned u32x2_s __attribute__((ext_vector_type(2))); u32x2_s w; w.x = cvt_pk_bf16(v[0], v[1]); w.y = cvt_pk_bf16(v[2], v[3]);
;                         *(u32x2_s*)(XB + ro + bj * HALF + n * 16) = w;
.LBB0_758:
	v_pk_add_f32 v[106:107], v[102:103], v[106:107]
	v_pk_add_f32 v[104:105], v[100:101], v[104:105]
	s_and_b64 vcc, exec, s[40:41]
	v_cvt_pk_bf16_f32 v100, v104, v105
	v_cvt_pk_bf16_f32 v101, v106, v107
	s_mov_b64 s[2:3], -1
	ds_write_b64 v234, v[100:101] offset:64
	s_cbranch_vccnz .LBB0_760
	v_mov_b32_e32 v100, v168
	v_mov_b32_e32 v101, v169
	v_mov_b32_e32 v102, v170
	v_mov_b32_e32 v103, v171
	s_mov_b64 s[2:3], 0

; __device__ __forceinline__ unsigned cvt_pk_bf16(float lo, float hi) { unsigned r; asm volatile("v_cvt_pk_bf16_f32 %0, %1, %2" : "=v"(r) : "v"(lo), "v"(hi)); return r; }
;     __device__ __forceinline__ void operator()(const f32x4 (&acc)[2][2][4][2], const Unit& u, int wr, int wc, int fr, int fq) const {
;     ...
;             for (int m = 0; m < 4; ++m) { const int row = row0 + ai * HALF + m * 16; const size_t ro = (size_t)row * 2048 + col0;
;                 float s = 0.f;
; #pragma unroll
;                 for (int bj = 0; bj < 2; ++bj)
; #pragma unroll
;                     for (int n = 0; n < 2; ++n) { f32x4 r;
;                         if (R32) r = *(const f32x4*)(R32 + ro + bj * HALF + n * 16);
;                         else { typedef unsigned u32x2_t __attribute__((ext_vector_type(2))); const u32x2_t rw = *(const u32x2_t*)(R16 + ro + bj * HALF + n * 16); const unsigned r0 = rw.x, r1 = rw.y;
;                             r = (f32x4){__builtin_bit_cast(float, r0 << 16), __builtin_bit_cast(float, r0 & 0xffff0000u), __builtin_bit_cast(float, r1 << 16), __builtin_bit_cast(float, r1 & 0xffff0000u)}; }
;                         const f32x4 v = acc[ai][bj][m][n] + r;
;                         typedef unsigned u32x2_s __attribute__((ext_vector_type(2))); u32x2_s w; w.x = cvt_pk_bf16(v[0], v[1]); w.y = cvt_pk_bf16(v[2], v[3]);
;                         *(u32x2_s*)(XB + ro + bj * HALF + n * 16) = w;
.LBB0_764:
	s_or_b64 exec, exec, s[2:3]
	v_or_b32_e32 v96, 32, v138
	s_waitcnt lgkmcnt(0)
	v_ashrrev_i32_e32 v97, 31, v96
	v_lshlrev_b64 v[96:97], 11, v[96:97]
	v_readlane_b32 s4, v252, 2
	v_lshl_add_u64 v[106:107], v[96:97], 0, v[142:143]
	v_readlane_b32 s5, v252, 3
	s_mov_b64 s[2:3], -1
	s_and_b64 vcc, exec, s[40:41]
	v_lshl_add_u64 v[100:101], v[106:107], 2, s[4:5]
	v_readlane_b32 s6, v252, 4
	v_readlane_b32 s7, v252, 5
	v_readlane_b32 s8, v252, 6
	v_readlane_b32 s9, v252, 7
	v_readlane_b32 s10, v252, 8
	v_readlane_b32 s11, v252, 9
	v_readlane_b32 s12, v252, 10
	v_readlane_b32 s13, v252, 11
	v_readlane_b32 s14, v252, 12
	v_readlane_b32 s15, v252, 13
	v_readlane_b32 s16, v252, 14
	v_readlane_b32 s17, v252, 15
	v_readlane_b32 s18, v252, 16
	v_readlane_b32 s19, v252, 17
	s_cbranch_vccnz .LBB0_766
	global_load_dwordx4 v[156:159], v[100:101], off
	global_load_dwordx4 v[160:163], v[100:101], off offset:64
	global_load_dwordx4 v[164:167], v[100:101], off offset:512
	global_load_dwordx4 v[168:171], v[100:101], off offset:576
	s_waitcnt vmcnt(0)
	v_mov_b32_e32 v96, v156
	v_mov_b32_e32 v97, v157
	v_mov_b32_e32 v98, v158
	v_mov_b32_e32 v99, v159
	s_mov_b64 s[2:3], 0

; __device__ __forceinline__ unsigned cvt_pk_bf16(float lo, float hi) { unsigned r; asm volatile("v_cvt_pk_bf16_f32 %0, %1, %2" : "=v"(r) : "v"(lo), "v"(hi)); return r; }
;     __device__ __forceinline__ void operator()(const f32x4 (&acc)[2][2][4][2], const Unit& u, int wr, int wc, int fr, int fq) const {
;     ...
;                     for (int n = 0; n < 2; ++n) { f32x4 r;
;                         if (R32) r = *(const f32x4*)(R32 + ro + bj * HALF + n * 16);
;                         else { typedef unsigned u32x2_t __attribute__((ext_vector_type(2))); const u32x2_t rw = *(const u32x2_t*)(R16 + ro + bj * HALF + n * 16); const unsigned r0 = rw.x, r1 = rw.y;
;                             r = (f32x4){__builtin_bit_cast(float, r0 << 16), __builtin_bit_cast(float, r0 & 0xffff0000u), __builtin_bit_cast(float, r1 << 16), __builtin_bit_cast(float, r1 & 0xffff0000u)}; }
;                         const f32x4 v = acc[ai][bj][m][n] + r;
;                         typedef unsigned u32x2_s __attribute__((ext_vector_type(2))); u32x2_s w; w.x = cvt_pk_bf16(v[0], v[1]); w.y = cvt_pk_bf16(v[2], v[3]);
;                         *(u32x2_s*)(XB + ro + bj * HALF + n * 16) = w;
.LBB0_768:
	v_pk_add_f32 v[98:99], v[94:95], v[98:99]
	v_pk_add_f32 v[104:105], v[92:93], v[96:97]
	v_lshl_add_u64 v[96:97], v[106:107], 1, s[90:91]
	v_cvt_pk_bf16_f32 v92, v104, v105
	v_cvt_pk_bf16_f32 v93, v98, v99
	s_and_b64 vcc, exec, s[40:41]
	s_mov_b64 s[2:3], -1
	ds_write_b64 v234, v[92:93]
	s_cbranch_vccnz .LBB0_770
	v_mov_b32_e32 v92, v160
	v_mov_b32_e32 v93, v161
	v_mov_b32_e32 v94, v162
	v_mov_b32_e32 v95, v163
	s_mov_b64 s[2:3], 0

; __device__ __forceinline__ unsigned cvt_pk_bf16(float lo, float hi) { unsigned r; asm volatile("v_cvt_pk_bf16_f32 %0, %1, %2" : "=v"(r) : "v"(lo), "v"(hi)); return r; }
;     __device__ __forceinline__ void operator()(const f32x4 (&acc)[2][2][4][2], const Unit& u, int wr, int wc, int fr, int fq) const {
;     ...
;                     for (int n = 0; n < 2; ++n) { f32x4 r;
;                         if (R32) r = *(const f32x4*)(R32 + ro + bj * HALF + n * 16);
;                         else { typedef unsigned u32x2_t __attribute__((ext_vector_type(2))); const u32x2_t rw = *(const u32x2_t*)(R16 + ro + bj * HALF + n * 16); const unsigned r0 = rw.x, r1 = rw.y;
;                             r = (f32x4){__builtin_bit_cast(float, r0 << 16), __builtin_bit_cast(float, r0 & 0xffff0000u), __builtin_bit_cast(float, r1 << 16), __builtin_bit_cast(float, r1 & 0xffff0000u)}; }
;                         const f32x4 v = acc[ai][bj][m][n] + r;
;                         typedef unsigned u32x2_s __attribute__((ext_vector_type(2))); u32x2_s w; w.x = cvt_pk_bf16(v[0], v[1]); w.y = cvt_pk_bf16(v[2], v[3]);
;                         *(u32x2_s*)(XB + ro + bj * HALF + n * 16) = w;
.LBB0_772:
	v_pk_add_f32 v[94:95], v[90:91], v[94:95]
	v_pk_add_f32 v[92:93], v[88:89], v[92:93]
	s_and_b64 vcc, exec, s[40:41]
	v_cvt_pk_bf16_f32 v88, v92, v93
	v_cvt_pk_bf16_f32 v89, v94, v95
	s_mov_b64 s[2:3], -1
	ds_write_b64 v234, v[88:89] offset:32
	s_cbranch_vccnz .LBB0_774
	v_mov_b32_e32 v88, v164
	v_mov_b32_e32 v89, v165
	v_mov_b32_e32 v90, v166
	v_mov_b32_e32 v91, v167
	s_mov_b64 s[2:3], 0

; __device__ __forceinline__ unsigned cvt_pk_bf16(float lo, float hi) { unsigned r; asm volatile("v_cvt_pk_bf16_f32 %0, %1, %2" : "=v"(r) : "v"(lo), "v"(hi)); return r; }
;     __device__ __forceinline__ void operator()(const f32x4 (&acc)[2][2][4][2], const Unit& u, int wr, int wc, int fr, int fq) const {
;     ...
;                     for (int n = 0; n < 2; ++n) { f32x4 r;
;                         if (R32) r = *(const f32x4*)(R32 + ro + bj * HALF + n * 16);
;                         else { typedef unsigned u32x2_t __attribute__((ext_vector_type(2))); const u32x2_t rw = *(const u32x2_t*)(R16 + ro + bj * HALF + n * 16); const unsigned r0 = rw.x, r1 = rw.y;
;                             r = (f32x4){__builtin_bit_cast(float, r0 << 16), __builtin_bit_cast(float, r0 & 0xffff0000u), __builtin_bit_cast(float, r1 << 16), __builtin_bit_cast(float, r1 & 0xffff0000u)}; }
;                         const f32x4 v = acc[ai][bj][m][n] + r;
;                         typedef unsigned u32x2_s __attribute__((ext_vector_type(2))); u32x2_s w; w.x = cvt_pk_bf16(v[0], v[1]); w.y = cvt_pk_bf16(v[2], v[3]);
;                         *(u32x2_s*)(XB + ro + bj * HALF + n * 16) = w;
.LBB0_776:
	v_pk_add_f32 v[90:91], v[86:87], v[90:91]
	v_pk_add_f32 v[88:89], v[84:85], v[88:89]
	s_and_b64 vcc, exec, s[40:41]
	v_cvt_pk_bf16_f32 v84, v88, v89
	v_cvt_pk_bf16_f32 v85, v90, v91
	s_mov_b64 s[2:3], -1
	ds_write_b64 v234, v[84:85] offset:64
	s_cbranch_vccnz .LBB0_778
	v_mov_b32_e32 v84, v168
	v_mov_b32_e32 v85, v169
	v_mov_b32_e32 v86, v170
	v_mov_b32_e32 v87, v171
	s_mov_b64 s[2:3], 0

; __device__ __forceinline__ unsigned cvt_pk_bf16(float lo, float hi) { unsigned r; asm volatile("v_cvt_pk_bf16_f32 %0, %1, %2" : "=v"(r) : "v"(lo), "v"(hi)); return r; }
;     __device__ __forceinline__ void operator()(const f32x4 (&acc)[2][2][4][2], const Unit& u, int wr, int wc, int fr, int fq) const {
;     ...
;             for (int m = 0; m < 4; ++m) { const int row = row0 + ai * HALF + m * 16; const size_t ro = (size_t)row * 2048 + col0;
;                 float s = 0.f;
; #pragma unroll
;                 for (int bj = 0; bj < 2; ++bj)
; #pragma unroll
;                     for (int n = 0; n < 2; ++n) { f32x4 r;
;                         if (R32) r = *(const f32x4*)(R32 + ro + bj * HALF + n * 16);
;                         else { typedef unsigned u32x2_t __attribute__((ext_vector_type(2))); const u32x2_t rw = *(const u32x2_t*)(R16 + ro + bj * HALF + n * 16); const unsigned r0 = rw.x, r1 = rw.y;
;                             r = (f32x4){__builtin_bit_cast(float, r0 << 16), __builtin_bit_cast(float, r0 & 0xffff0000u), __builtin_bit_cast(float, r1 << 16), __builtin_bit_cast(float, r1 & 0xffff0000u)}; }
;                         const f32x4 v = acc[ai][bj][m][n] + r;
;                         typedef unsigned u32x2_s __attribute__((ext_vector_type(2))); u32x2_s w; w.x = cvt_pk_bf16(v[0], v[1]); w.y = cvt_pk_bf16(v[2], v[3]);
;                         *(u32x2_s*)(XB + ro + bj * HALF + n * 16) = w;
.LBB0_782:
	s_or_b64 exec, exec, s[2:3]
	v_or_b32_e32 v80, 48, v138
	s_waitcnt lgkmcnt(0)
	v_ashrrev_i32_e32 v81, 31, v80
	v_lshlrev_b64 v[80:81], 11, v[80:81]
	v_readlane_b32 s4, v252, 2
	v_lshl_add_u64 v[90:91], v[80:81], 0, v[142:143]
	v_readlane_b32 s5, v252, 3
	s_mov_b64 s[2:3], -1
	s_and_b64 vcc, exec, s[40:41]
	v_lshl_add_u64 v[84:85], v[90:91], 2, s[4:5]
	v_readlane_b32 s6, v252, 4
	v_readlane_b32 s7, v252, 5
	v_readlane_b32 s8, v252, 6
	v_readlane_b32 s9, v252, 7
	v_readlane_b32 s10, v252, 8
	v_readlane_b32 s11, v252, 9
	v_readlane_b32 s12, v252, 10
	v_readlane_b32 s13, v252, 11
	v_readlane_b32 s14, v252, 12
	v_readlane_b32 s15, v252, 13
	v_readlane_b32 s16, v252, 14
	v_readlane_b32 s17, v252, 15
	v_readlane_b32 s18, v252, 16
	v_readlane_b32 s19, v252, 17
	s_cbranch_vccnz .LBB0_784
	global_load_dwordx4 v[156:159], v[84:85], off
	global_load_dwordx4 v[160:163], v[84:85], off offset:64
	global_load_dwordx4 v[164:167], v[84:85], off offset:512
	global_load_dwordx4 v[168:171], v[84:85], off offset:576
	s_waitcnt vmcnt(0)
	v_mov_b32_e32 v80, v156
	v_mov_b32_e32 v81, v157
	v_mov_b32_e32 v82, v158
	v_mov_b32_e32 v83, v159
	s_mov_b64 s[2:3], 0

; __device__ __forceinline__ unsigned cvt_pk_bf16(float lo, float hi) { unsigned r; asm volatile("v_cvt_pk_bf16_f32 %0, %1, %2" : "=v"(r) : "v"(lo), "v"(hi)); return r; }
;     __device__ __forceinline__ void operator()(const f32x4 (&acc)[2][2][4][2], const Unit& u, int wr, int wc, int fr, int fq) const {
;     ...
;                     for (int n = 0; n < 2; ++n) { f32x4 r;
;                         if (R32) r = *(const f32x4*)(R32 + ro + bj * HALF + n * 16);
;                         else { typedef unsigned u32x2_t __attribute__((ext_vector_type(2))); const u32x2_t rw = *(const u32x2_t*)(R16 + ro + bj * HALF + n * 16); const unsigned r0 = rw.x, r1 = rw.y;
;                             r = (f32x4){__builtin_bit_cast(float, r0 << 16), __builtin_bit_cast(float, r0 & 0xffff0000u), __builtin_bit_cast(float, r1 << 16), __builtin_bit_cast(float, r1 & 0xffff0000u)}; }
;                         const f32x4 v = acc[ai][bj][m][n] + r;
;                         typedef unsigned u32x2_s __attribute__((ext_vector_type(2))); u32x2_s w; w.x = cvt_pk_bf16(v[0], v[1]); w.y = cvt_pk_bf16(v[2], v[3]);
;                         *(u32x2_s*)(XB + ro + bj * HALF + n * 16) = w;
.LBB0_786:
	v_pk_add_f32 v[82:83], v[78:79], v[82:83]
	v_pk_add_f32 v[88:89], v[76:77], v[80:81]
	v_lshl_add_u64 v[80:81], v[90:91], 1, s[90:91]
	v_cvt_pk_bf16_f32 v76, v88, v89
	v_cvt_pk_bf16_f32 v77, v82, v83
	s_and_b64 vcc, exec, s[40:41]
	s_mov_b64 s[2:3], -1
	ds_write_b64 v234, v[76:77]
	s_cbranch_vccnz .LBB0_788
	v_mov_b32_e32 v76, v160
	v_mov_b32_e32 v77, v161
	v_mov_b32_e32 v78, v162
	v_mov_b32_e32 v79, v163
	s_mov_b64 s[2:3], 0

; __device__ __forceinline__ unsigned cvt_pk_bf16(float lo, float hi) { unsigned r; asm volatile("v_cvt_pk_bf16_f32 %0, %1, %2" : "=v"(r) : "v"(lo), "v"(hi)); return r; }
;     __device__ __forceinline__ void operator()(const f32x4 (&acc)[2][2][4][2], const Unit& u, int wr, int wc, int fr, int fq) const {
;     ...
;                     for (int n = 0; n < 2; ++n) { f32x4 r;
;                         if (R32) r = *(const f32x4*)(R32 + ro + bj * HALF + n * 16);
;                         else { typedef unsigned u32x2_t __attribute__((ext_vector_type(2))); const u32x2_t rw = *(const u32x2_t*)(R16 + ro + bj * HALF + n * 16); const unsigned r0 = rw.x, r1 = rw.y;
;                             r = (f32x4){__builtin_bit_cast(float, r0 << 16), __builtin_bit_cast(float, r0 & 0xffff0000u), __builtin_bit_cast(float, r1 << 16), __builtin_bit_cast(float, r1 & 0xffff0000u)}; }
;                         const f32x4 v = acc[ai][bj][m][n] + r;
;                         typedef unsigned u32x2_s __attribute__((ext_vector_type(2))); u32x2_s w; w.x = cvt_pk_bf16(v[0], v[1]); w.y = cvt_pk_bf16(v[2], v[3]);
;                         *(u32x2_s*)(XB + ro + bj * HALF + n * 16) = w;
.LBB0_790:
	v_pk_add_f32 v[78:79], v[74:75], v[78:79]
	v_pk_add_f32 v[76:77], v[72:73], v[76:77]
	s_and_b64 vcc, exec, s[40:41]
	v_cvt_pk_bf16_f32 v72, v76, v77
	v_cvt_pk_bf16_f32 v73, v78, v79
	s_mov_b64 s[2:3], -1
	ds_write_b64 v234, v[72:73] offset:32
	s_cbranch_vccnz .LBB0_792
	v_mov_b32_e32 v72, v164
	v_mov_b32_e32 v73, v165
	v_mov_b32_e32 v74, v166
	v_mov_b32_e32 v75, v167
	s_mov_b64 s[2:3], 0

; __device__ __forceinline__ unsigned cvt_pk_bf16(float lo, float hi) { unsigned r; asm volatile("v_cvt_pk_bf16_f32 %0, %1, %2" : "=v"(r) : "v"(lo), "v"(hi)); return r; }
;     __device__ __forceinline__ void operator()(const f32x4 (&acc)[2][2][4][2], const Unit& u, int wr, int wc, int fr, int fq) const {
;     ...
;                     for (int n = 0; n < 2; ++n) { f32x4 r;
;                         if (R32) r = *(const f32x4*)(R32 + ro + bj * HALF + n * 16);
;                         else { typedef unsigned u32x2_t __attribute__((ext_vector_type(2))); const u32x2_t rw = *(const u32x2_t*)(R16 + ro + bj * HALF + n * 16); const unsigned r0 = rw.x, r1 = rw.y;
;                             r = (f32x4){__builtin_bit_cast(float, r0 << 16), __builtin_bit_cast(float, r0 & 0xffff0000u), __builtin_bit_cast(float, r1 << 16), __builtin_bit_cast(float, r1 & 0xffff0000u)}; }
;                         const f32x4 v = acc[ai][bj][m][n] + r;
;                         typedef unsigned u32x2_s __attribute__((ext_vector_type(2))); u32x2_s w; w.x = cvt_pk_bf16(v[0], v[1]); w.y = cvt_pk_bf16(v[2], v[3]);
;                         *(u32x2_s*)(XB + ro + bj * HALF + n * 16) = w;
.LBB0_794:
	v_pk_add_f32 v[74:75], v[70:71], v[74:75]
	v_pk_add_f32 v[72:73], v[68:69], v[72:73]
	s_and_b64 vcc, exec, s[40:41]
	v_cvt_pk_bf16_f32 v68, v72, v73
	v_cvt_pk_bf16_f32 v69, v74, v75
	s_mov_b64 s[2:3], -1
	ds_write_b64 v234, v[68:69] offset:64
	s_cbranch_vccnz .LBB0_796
	v_mov_b32_e32 v68, v168
	v_mov_b32_e32 v69, v169
	v_mov_b32_e32 v70, v170
	v_mov_b32_e32 v71, v171
	s_mov_b64 s[2:3], 0

; __device__ __forceinline__ unsigned cvt_pk_bf16(float lo, float hi) { unsigned r; asm volatile("v_cvt_pk_bf16_f32 %0, %1, %2" : "=v"(r) : "v"(lo), "v"(hi)); return r; }
;     __device__ __forceinline__ void operator()(const f32x4 (&acc)[2][2][4][2], const Unit& u, int wr, int wc, int fr, int fq) const {
;     ...
;             for (int m = 0; m < 4; ++m) { const int row = row0 + ai * HALF + m * 16; const size_t ro = (size_t)row * 2048 + col0;
;                 float s = 0.f;
; #pragma unroll
;                 for (int bj = 0; bj < 2; ++bj)
; #pragma unroll
;                     for (int n = 0; n < 2; ++n) { f32x4 r;
;                         if (R32) r = *(const f32x4*)(R32 + ro + bj * HALF + n * 16);
;                         else { typedef unsigned u32x2_t __attribute__((ext_vector_type(2))); const u32x2_t rw = *(const u32x2_t*)(R16 + ro + bj * HALF + n * 16); const unsigned r0 = rw.x, r1 = rw.y;
;                             r = (f32x4){__builtin_bit_cast(float, r0 << 16), __builtin_bit_cast(float, r0 & 0xffff0000u), __builtin_bit_cast(float, r1 << 16), __builtin_bit_cast(float, r1 & 0xffff0000u)}; }
;                         const f32x4 v = acc[ai][bj][m][n] + r;
;                         typedef unsigned u32x2_s __attribute__((ext_vector_type(2))); u32x2_s w; w.x = cvt_pk_bf16(v[0], v[1]); w.y = cvt_pk_bf16(v[2], v[3]);
;                         *(u32x2_s*)(XB + ro + bj * HALF + n * 16) = w;
.LBB0_800:
	s_or_b64 exec, exec, s[2:3]
	s_mov_b64 s[2:3], 0x40000
	v_readlane_b32 s4, v252, 2
	v_lshl_add_u64 v[74:75], v[140:141], 0, s[2:3]
	v_readlane_b32 s5, v252, 3
	s_mov_b64 s[2:3], -1
	s_and_b64 vcc, exec, s[40:41]
	v_lshl_add_u64 v[68:69], v[74:75], 2, s[4:5]
	v_readlane_b32 s6, v252, 4
	v_readlane_b32 s7, v252, 5
	v_readlane_b32 s8, v252, 6
	v_readlane_b32 s9, v252, 7
	v_readlane_b32 s10, v252, 8
	v_readlane_b32 s11, v252, 9
	v_readlane_b32 s12, v252, 10
	v_readlane_b32 s13, v252, 11
	v_readlane_b32 s14, v252, 12
	v_readlane_b32 s15, v252, 13
	v_readlane_b32 s16, v252, 14
	v_readlane_b32 s17, v252, 15
	v_readlane_b32 s18, v252, 16
	v_readlane_b32 s19, v252, 17
	s_cbranch_vccnz .LBB0_802
	s_waitcnt lgkmcnt(0)
	global_load_dwordx4 v[156:159], v[68:69], off
	global_load_dwordx4 v[160:163], v[68:69], off offset:64
	global_load_dwordx4 v[164:167], v[68:69], off offset:512
	global_load_dwordx4 v[168:171], v[68:69], off offset:576
	s_waitcnt vmcnt(0)
	v_mov_b32_e32 v64, v156
	v_mov_b32_e32 v65, v157
	v_mov_b32_e32 v66, v158
	v_mov_b32_e32 v67, v159
	s_mov_b64 s[2:3], 0

; __device__ __forceinline__ unsigned cvt_pk_bf16(float lo, float hi) { unsigned r; asm volatile("v_cvt_pk_bf16_f32 %0, %1, %2" : "=v"(r) : "v"(lo), "v"(hi)); return r; }
;     __device__ __forceinline__ void operator()(const f32x4 (&acc)[2][2][4][2], const Unit& u, int wr, int wc, int fr, int fq) const {
;     ...
;                     for (int n = 0; n < 2; ++n) { f32x4 r;
;                         if (R32) r = *(const f32x4*)(R32 + ro + bj * HALF + n * 16);
;                         else { typedef unsigned u32x2_t __attribute__((ext_vector_type(2))); const u32x2_t rw = *(const u32x2_t*)(R16 + ro + bj * HALF + n * 16); const unsigned r0 = rw.x, r1 = rw.y;
;                             r = (f32x4){__builtin_bit_cast(float, r0 << 16), __builtin_bit_cast(float, r0 & 0xffff0000u), __builtin_bit_cast(float, r1 << 16), __builtin_bit_cast(float, r1 & 0xffff0000u)}; }
;                         const f32x4 v = acc[ai][bj][m][n] + r;
;                         typedef unsigned u32x2_s __attribute__((ext_vector_type(2))); u32x2_s w; w.x = cvt_pk_bf16(v[0], v[1]); w.y = cvt_pk_bf16(v[2], v[3]);
;                         *(u32x2_s*)(XB + ro + bj * HALF + n * 16) = w;
.LBB0_804:
	v_pk_add_f32 v[66:67], v[62:63], v[66:67]
	s_waitcnt lgkmcnt(0)
	v_pk_add_f32 v[72:73], v[60:61], v[64:65]
	v_lshl_add_u64 v[64:65], v[74:75], 1, s[90:91]
	v_cvt_pk_bf16_f32 v60, v72, v73
	v_cvt_pk_bf16_f32 v61, v66, v67
	s_and_b64 vcc, exec, s[40:41]
	s_mov_b64 s[2:3], -1
	ds_write_b64 v234, v[60:61]
	s_cbranch_vccnz .LBB0_806
	v_mov_b32_e32 v60, v160
	v_mov_b32_e32 v61, v161
	v_mov_b32_e32 v62, v162
	v_mov_b32_e32 v63, v163
	s_mov_b64 s[2:3], 0

; __device__ __forceinline__ unsigned cvt_pk_bf16(float lo, float hi) { unsigned r; asm volatile("v_cvt_pk_bf16_f32 %0, %1, %2" : "=v"(r) : "v"(lo), "v"(hi)); return r; }
;     __device__ __forceinline__ void operator()(const f32x4 (&acc)[2][2][4][2], const Unit& u, int wr, int wc, int fr, int fq) const {
;     ...
;                     for (int n = 0; n < 2; ++n) { f32x4 r;
;                         if (R32) r = *(const f32x4*)(R32 + ro + bj * HALF + n * 16);
;                         else { typedef unsigned u32x2_t __attribute__((ext_vector_type(2))); const u32x2_t rw = *(const u32x2_t*)(R16 + ro + bj * HALF + n * 16); const unsigned r0 = rw.x, r1 = rw.y;
;                             r = (f32x4){__builtin_bit_cast(float, r0 << 16), __builtin_bit_cast(float, r0 & 0xffff0000u), __builtin_bit_cast(float, r1 << 16), __builtin_bit_cast(float, r1 & 0xffff0000u)}; }
;                         const f32x4 v = acc[ai][bj][m][n] + r;
;                         typedef unsigned u32x2_s __attribute__((ext_vector_type(2))); u32x2_s w; w.x = cvt_pk_bf16(v[0], v[1]); w.y = cvt_pk_bf16(v[2], v[3]);
;                         *(u32x2_s*)(XB + ro + bj * HALF + n * 16) = w;
.LBB0_808:
	v_pk_add_f32 v[62:63], v[58:59], v[62:63]
	v_pk_add_f32 v[60:61], v[56:57], v[60:61]
	s_and_b64 vcc, exec, s[40:41]
	v_cvt_pk_bf16_f32 v56, v60, v61
	v_cvt_pk_bf16_f32 v57, v62, v63
	s_mov_b64 s[2:3], -1
	ds_write_b64 v234, v[56:57] offset:32
	s_cbranch_vccnz .LBB0_810
	v_mov_b32_e32 v56, v164
	v_mov_b32_e32 v57, v165
	v_mov_b32_e32 v58, v166
	v_mov_b32_e32 v59, v167
	s_mov_b64 s[2:3], 0

; __device__ __forceinline__ unsigned cvt_pk_bf16(float lo, float hi) { unsigned r; asm volatile("v_cvt_pk_bf16_f32 %0, %1, %2" : "=v"(r) : "v"(lo), "v"(hi)); return r; }
;     __device__ __forceinline__ void operator()(const f32x4 (&acc)[2][2][4][2], const Unit& u, int wr, int wc, int fr, int fq) const {
;     ...
;                     for (int n = 0; n < 2; ++n) { f32x4 r;
;                         if (R32) r = *(const f32x4*)(R32 + ro + bj * HALF + n * 16);
;                         else { typedef unsigned u32x2_t __attribute__((ext_vector_type(2))); const u32x2_t rw = *(const u32x2_t*)(R16 + ro + bj * HALF + n * 16); const unsigned r0 = rw.x, r1 = rw.y;
;                             r = (f32x4){__builtin_bit_cast(float, r0 << 16), __builtin_bit_cast(float, r0 & 0xffff0000u), __builtin_bit_cast(float, r1 << 16), __builtin_bit_cast(float, r1 & 0xffff0000u)}; }
;                         const f32x4 v = acc[ai][bj][m][n] + r;
;                         typedef unsigned u32x2_s __attribute__((ext_vector_type(2))); u32x2_s w; w.x = cvt_pk_bf16(v[0], v[1]); w.y = cvt_pk_bf16(v[2], v[3]);
;                         *(u32x2_s*)(XB + ro + bj * HALF + n * 16) = w;
.LBB0_812:
	v_pk_add_f32 v[58:59], v[54:55], v[58:59]
	v_pk_add_f32 v[56:57], v[52:53], v[56:57]
	s_and_b64 vcc, exec, s[40:41]
	v_cvt_pk_bf16_f32 v52, v56, v57
	v_cvt_pk_bf16_f32 v53, v58, v59
	s_mov_b64 s[2:3], -1
	ds_write_b64 v234, v[52:53] offset:64
	s_cbranch_vccnz .LBB0_814
	v_mov_b32_e32 v52, v168
	v_mov_b32_e32 v53, v169
	v_mov_b32_e32 v54, v170
	v_mov_b32_e32 v55, v171
	s_mov_b64 s[2:3], 0

; __device__ __forceinline__ unsigned cvt_pk_bf16(float lo, float hi) { unsigned r; asm volatile("v_cvt_pk_bf16_f32 %0, %1, %2" : "=v"(r) : "v"(lo), "v"(hi)); return r; }
;     __device__ __forceinline__ void operator()(const f32x4 (&acc)[2][2][4][2], const Unit& u, int wr, int wc, int fr, int fq) const {
;     ...
;             for (int m = 0; m < 4; ++m) { const int row = row0 + ai * HALF + m * 16; const size_t ro = (size_t)row * 2048 + col0;
;                 float s = 0.f;
; #pragma unroll
;                 for (int bj = 0; bj < 2; ++bj)
; #pragma unroll
;                     for (int n = 0; n < 2; ++n) { f32x4 r;
;                         if (R32) r = *(const f32x4*)(R32 + ro + bj * HALF + n * 16);
;                         else { typedef unsigned u32x2_t __attribute__((ext_vector_type(2))); const u32x2_t rw = *(const u32x2_t*)(R16 + ro + bj * HALF + n * 16); const unsigned r0 = rw.x, r1 = rw.y;
;                             r = (f32x4){__builtin_bit_cast(float, r0 << 16), __builtin_bit_cast(float, r0 & 0xffff0000u), __builtin_bit_cast(float, r1 << 16), __builtin_bit_cast(float, r1 & 0xffff0000u)}; }
;                         const f32x4 v = acc[ai][bj][m][n] + r;
;                         typedef unsigned u32x2_s __attribute__((ext_vector_type(2))); u32x2_s w; w.x = cvt_pk_bf16(v[0], v[1]); w.y = cvt_pk_bf16(v[2], v[3]);
;                         *(u32x2_s*)(XB + ro + bj * HALF + n * 16) = w;
.LBB0_818:
	s_or_b64 exec, exec, s[2:3]
	s_mov_b64 s[2:3], 0x48000
	v_readlane_b32 s4, v252, 2
	v_lshl_add_u64 v[58:59], v[140:141], 0, s[2:3]
	v_readlane_b32 s5, v252, 3
	s_mov_b64 s[2:3], -1
	s_and_b64 vcc, exec, s[40:41]
	v_lshl_add_u64 v[52:53], v[58:59], 2, s[4:5]
	v_readlane_b32 s6, v252, 4
	v_readlane_b32 s7, v252, 5
	v_readlane_b32 s8, v252, 6
	v_readlane_b32 s9, v252, 7
	v_readlane_b32 s10, v252, 8
	v_readlane_b32 s11, v252, 9
	v_readlane_b32 s12, v252, 10
	v_readlane_b32 s13, v252, 11
	v_readlane_b32 s14, v252, 12
	v_readlane_b32 s15, v252, 13
	v_readlane_b32 s16, v252, 14
	v_readlane_b32 s17, v252, 15
	v_readlane_b32 s18, v252, 16
	v_readlane_b32 s19, v252, 17
	s_cbranch_vccnz .LBB0_820
	s_waitcnt lgkmcnt(0)
	global_load_dwordx4 v[156:159], v[52:53], off
	global_load_dwordx4 v[160:163], v[52:53], off offset:64
	global_load_dwordx4 v[164:167], v[52:53], off offset:512
	global_load_dwordx4 v[168:171], v[52:53], off offset:576
	s_waitcnt vmcnt(0)
	v_mov_b32_e32 v48, v156
	v_mov_b32_e32 v49, v157
	v_mov_b32_e32 v50, v158
	v_mov_b32_e32 v51, v159
	s_mov_b64 s[2:3], 0

; __device__ __forceinline__ unsigned cvt_pk_bf16(float lo, float hi) { unsigned r; asm volatile("v_cvt_pk_bf16_f32 %0, %1, %2" : "=v"(r) : "v"(lo), "v"(hi)); return r; }
;     __device__ __forceinline__ void operator()(const f32x4 (&acc)[2][2][4][2], const Unit& u, int wr, int wc, int fr, int fq) const {
;     ...
;                     for (int n = 0; n < 2; ++n) { f32x4 r;
;                         if (R32) r = *(const f32x4*)(R32 + ro + bj * HALF + n * 16);
;                         else { typedef unsigned u32x2_t __attribute__((ext_vector_type(2))); const u32x2_t rw = *(const u32x2_t*)(R16 + ro + bj * HALF + n * 16); const unsigned r0 = rw.x, r1 = rw.y;
;                             r = (f32x4){__builtin_bit_cast(float, r0 << 16), __builtin_bit_cast(float, r0 & 0xffff0000u), __builtin_bit_cast(float, r1 << 16), __builtin_bit_cast(float, r1 & 0xffff0000u)}; }
;                         const f32x4 v = acc[ai][bj][m][n] + r;
;                         typedef unsigned u32x2_s __attribute__((ext_vector_type(2))); u32x2_s w; w.x = cvt_pk_bf16(v[0], v[1]); w.y = cvt_pk_bf16(v[2], v[3]);
;                         *(u32x2_s*)(XB + ro + bj * HALF + n * 16) = w;
.LBB0_822:
	v_pk_add_f32 v[50:51], v[46:47], v[50:51]
	s_waitcnt lgkmcnt(0)
	v_pk_add_f32 v[56:57], v[44:45], v[48:49]
	v_lshl_add_u64 v[48:49], v[58:59], 1, s[90:91]
	v_cvt_pk_bf16_f32 v44, v56, v57
	v_cvt_pk_bf16_f32 v45, v50, v51
	s_and_b64 vcc, exec, s[40:41]
	s_mov_b64 s[2:3], -1
	ds_write_b64 v234, v[44:45]
	s_cbranch_vccnz .LBB0_824
	v_mov_b32_e32 v44, v160
	v_mov_b32_e32 v45, v161
	v_mov_b32_e32 v46, v162
	v_mov_b32_e32 v47, v163
	s_mov_b64 s[2:3], 0

; __device__ __forceinline__ unsigned cvt_pk_bf16(float lo, float hi) { unsigned r; asm volatile("v_cvt_pk_bf16_f32 %0, %1, %2" : "=v"(r) : "v"(lo), "v"(hi)); return r; }
;     __device__ __forceinline__ void operator()(const f32x4 (&acc)[2][2][4][2], const Unit& u, int wr, int wc, int fr, int fq) const {
;     ...
;                     for (int n = 0; n < 2; ++n) { f32x4 r;
;                         if (R32) r = *(const f32x4*)(R32 + ro + bj * HALF + n * 16);
;                         else { typedef unsigned u32x2_t __attribute__((ext_vector_type(2))); const u32x2_t rw = *(const u32x2_t*)(R16 + ro + bj * HALF + n * 16); const unsigned r0 = rw.x, r1 = rw.y;
;                             r = (f32x4){__builtin_bit_cast(float, r0 << 16), __builtin_bit_cast(float, r0 & 0xffff0000u), __builtin_bit_cast(float, r1 << 16), __builtin_bit_cast(float, r1 & 0xffff0000u)}; }
;                         const f32x4 v = acc[ai][bj][m][n] + r;
;                         typedef unsigned u32x2_s __attribute__((ext_vector_type(2))); u32x2_s w; w.x = cvt_pk_bf16(v[0], v[1]); w.y = cvt_pk_bf16(v[2], v[3]);
;                         *(u32x2_s*)(XB + ro + bj * HALF + n * 16) = w;
.LBB0_826:
	v_pk_add_f32 v[46:47], v[42:43], v[46:47]
	v_pk_add_f32 v[44:45], v[40:41], v[44:45]
	s_and_b64 vcc, exec, s[40:41]
	v_cvt_pk_bf16_f32 v40, v44, v45
	v_cvt_pk_bf16_f32 v41, v46, v47
	s_mov_b64 s[2:3], -1
	ds_write_b64 v234, v[40:41] offset:32
	s_cbranch_vccnz .LBB0_828
	v_mov_b32_e32 v40, v164
	v_mov_b32_e32 v41, v165
	v_mov_b32_e32 v42, v166
	v_mov_b32_e32 v43, v167
	s_mov_b64 s[2:3], 0

; __device__ __forceinline__ unsigned cvt_pk_bf16(float lo, float hi) { unsigned r; asm volatile("v_cvt_pk_bf16_f32 %0, %1, %2" : "=v"(r) : "v"(lo), "v"(hi)); return r; }
;     __device__ __forceinline__ void operator()(const f32x4 (&acc)[2][2][4][2], const Unit& u, int wr, int wc, int fr, int fq) const {
;     ...
;                     for (int n = 0; n < 2; ++n) { f32x4 r;
;                         if (R32) r = *(const f32x4*)(R32 + ro + bj * HALF + n * 16);
;                         else { typedef unsigned u32x2_t __attribute__((ext_vector_type(2))); const u32x2_t rw = *(const u32x2_t*)(R16 + ro + bj * HALF + n * 16); const unsigned r0 = rw.x, r1 = rw.y;
;                             r = (f32x4){__builtin_bit_cast(float, r0 << 16), __builtin_bit_cast(float, r0 & 0xffff0000u), __builtin_bit_cast(float, r1 << 16), __builtin_bit_cast(float, r1 & 0xffff0000u)}; }
;                         const f32x4 v = acc[ai][bj][m][n] + r;
;                         typedef unsigned u32x2_s __attribute__((ext_vector_type(2))); u32x2_s w; w.x = cvt_pk_bf16(v[0], v[1]); w.y = cvt_pk_bf16(v[2], v[3]);
;                         *(u32x2_s*)(XB + ro + bj * HALF + n * 16) = w;
.LBB0_830:
	v_pk_add_f32 v[42:43], v[38:39], v[42:43]
	v_pk_add_f32 v[40:41], v[36:37], v[40:41]
	s_and_b64 vcc, exec, s[40:41]
	v_cvt_pk_bf16_f32 v36, v40, v41
	v_cvt_pk_bf16_f32 v37, v42, v43
	s_mov_b64 s[2:3], -1
	ds_write_b64 v234, v[36:37] offset:64
	s_cbranch_vccnz .LBB0_832
	v_mov_b32_e32 v36, v168
	v_mov_b32_e32 v37, v169
	v_mov_b32_e32 v38, v170
	v_mov_b32_e32 v39, v171
	s_mov_b64 s[2:3], 0

; __device__ __forceinline__ unsigned cvt_pk_bf16(float lo, float hi) { unsigned r; asm volatile("v_cvt_pk_bf16_f32 %0, %1, %2" : "=v"(r) : "v"(lo), "v"(hi)); return r; }
;     __device__ __forceinline__ void operator()(const f32x4 (&acc)[2][2][4][2], const Unit& u, int wr, int wc, int fr, int fq) const {
;     ...
;             for (int m = 0; m < 4; ++m) { const int row = row0 + ai * HALF + m * 16; const size_t ro = (size_t)row * 2048 + col0;
;                 float s = 0.f;
; #pragma unroll
;                 for (int bj = 0; bj < 2; ++bj)
; #pragma unroll
;                     for (int n = 0; n < 2; ++n) { f32x4 r;
;                         if (R32) r = *(const f32x4*)(R32 + ro + bj * HALF + n * 16);
;                         else { typedef unsigned u32x2_t __attribute__((ext_vector_type(2))); const u32x2_t rw = *(const u32x2_t*)(R16 + ro + bj * HALF + n * 16); const unsigned r0 = rw.x, r1 = rw.y;
;                             r = (f32x4){__builtin_bit_cast(float, r0 << 16), __builtin_bit_cast(float, r0 & 0xffff0000u), __builtin_bit_cast(float, r1 << 16), __builtin_bit_cast(float, r1 & 0xffff0000u)}; }
;                         const f32x4 v = acc[ai][bj][m][n] + r;
;                         typedef unsigned u32x2_s __attribute__((ext_vector_type(2))); u32x2_s w; w.x = cvt_pk_bf16(v[0], v[1]); w.y = cvt_pk_bf16(v[2], v[3]);
;                         *(u32x2_s*)(XB + ro + bj * HALF + n * 16) = w;
.LBB0_836:
	s_or_b64 exec, exec, s[2:3]
	s_mov_b64 s[2:3], 0x50000
	v_readlane_b32 s4, v252, 2
	v_lshl_add_u64 v[42:43], v[140:141], 0, s[2:3]
	v_readlane_b32 s5, v252, 3
	s_mov_b64 s[2:3], -1
	s_and_b64 vcc, exec, s[40:41]
	v_lshl_add_u64 v[36:37], v[42:43], 2, s[4:5]
	v_readlane_b32 s6, v252, 4
	v_readlane_b32 s7, v252, 5
	v_readlane_b32 s8, v252, 6
	v_readlane_b32 s9, v252, 7
	v_readlane_b32 s10, v252, 8
	v_readlane_b32 s11, v252, 9
	v_readlane_b32 s12, v252, 10
	v_readlane_b32 s13, v252, 11
	v_readlane_b32 s14, v252, 12
	v_readlane_b32 s15, v252, 13
	v_readlane_b32 s16, v252, 14
	v_readlane_b32 s17, v252, 15
	v_readlane_b32 s18, v252, 16
	v_readlane_b32 s19, v252, 17
	s_cbranch_vccnz .LBB0_838
	s_waitcnt lgkmcnt(0)
	global_load_dwordx4 v[156:159], v[36:37], off
	global_load_dwordx4 v[160:163], v[36:37], off offset:64
	global_load_dwordx4 v[164:167], v[36:37], off offset:512
	global_load_dwordx4 v[168:171], v[36:37], off offset:576
	s_waitcnt vmcnt(0)
	v_mov_b32_e32 v32, v156
	v_mov_b32_e32 v33, v157
	v_mov_b32_e32 v34, v158
	v_mov_b32_e32 v35, v159
	s_mov_b64 s[2:3], 0

; __device__ __forceinline__ unsigned cvt_pk_bf16(float lo, float hi) { unsigned r; asm volatile("v_cvt_pk_bf16_f32 %0, %1, %2" : "=v"(r) : "v"(lo), "v"(hi)); return r; }
;     __device__ __forceinline__ void operator()(const f32x4 (&acc)[2][2][4][2], const Unit& u, int wr, int wc, int fr, int fq) const {
;     ...
;                     for (int n = 0; n < 2; ++n) { f32x4 r;
;                         if (R32) r = *(const f32x4*)(R32 + ro + bj * HALF + n * 16);
;                         else { typedef unsigned u32x2_t __attribute__((ext_vector_type(2))); const u32x2_t rw = *(const u32x2_t*)(R16 + ro + bj * HALF + n * 16); const unsigned r0 = rw.x, r1 = rw.y;
;                             r = (f32x4){__builtin_bit_cast(float, r0 << 16), __builtin_bit_cast(float, r0 & 0xffff0000u), __builtin_bit_cast(float, r1 << 16), __builtin_bit_cast(float, r1 & 0xffff0000u)}; }
;                         const f32x4 v = acc[ai][bj][m][n] + r;
;                         typedef unsigned u32x2_s __attribute__((ext_vector_type(2))); u32x2_s w; w.x = cvt_pk_bf16(v[0], v[1]); w.y = cvt_pk_bf16(v[2], v[3]);
;                         *(u32x2_s*)(XB + ro + bj * HALF + n * 16) = w;
.LBB0_840:
	v_pk_add_f32 v[34:35], v[30:31], v[34:35]
	s_waitcnt lgkmcnt(0)
	v_pk_add_f32 v[40:41], v[28:29], v[32:33]
	v_lshl_add_u64 v[32:33], v[42:43], 1, s[90:91]
	v_cvt_pk_bf16_f32 v28, v40, v41
	v_cvt_pk_bf16_f32 v29, v34, v35
	s_and_b64 vcc, exec, s[40:41]
	s_mov_b64 s[2:3], -1
	ds_write_b64 v234, v[28:29]
	s_cbranch_vccnz .LBB0_842
	v_mov_b32_e32 v28, v160
	v_mov_b32_e32 v29, v161
	v_mov_b32_e32 v30, v162
	v_mov_b32_e32 v31, v163
	s_mov_b64 s[2:3], 0

; __device__ __forceinline__ unsigned cvt_pk_bf16(float lo, float hi) { unsigned r; asm volatile("v_cvt_pk_bf16_f32 %0, %1, %2" : "=v"(r) : "v"(lo), "v"(hi)); return r; }
;     __device__ __forceinline__ void operator()(const f32x4 (&acc)[2][2][4][2], const Unit& u, int wr, int wc, int fr, int fq) const {
;     ...
;                     for (int n = 0; n < 2; ++n) { f32x4 r;
;                         if (R32) r = *(const f32x4*)(R32 + ro + bj * HALF + n * 16);
;                         else { typedef unsigned u32x2_t __attribute__((ext_vector_type(2))); const u32x2_t rw = *(const u32x2_t*)(R16 + ro + bj * HALF + n * 16); const unsigned r0 = rw.x, r1 = rw.y;
;                             r = (f32x4){__builtin_bit_cast(float, r0 << 16), __builtin_bit_cast(float, r0 & 0xffff0000u), __builtin_bit_cast(float, r1 << 16), __builtin_bit_cast(float, r1 & 0xffff0000u)}; }
;                         const f32x4 v = acc[ai][bj][m][n] + r;
;                         typedef unsigned u32x2_s __attribute__((ext_vector_type(2))); u32x2_s w; w.x = cvt_pk_bf16(v[0], v[1]); w.y = cvt_pk_bf16(v[2], v[3]);
;                         *(u32x2_s*)(XB + ro + bj * HALF + n * 16) = w;
.LBB0_844:
	v_pk_add_f32 v[30:31], v[26:27], v[30:31]
	v_pk_add_f32 v[28:29], v[24:25], v[28:29]
	s_and_b64 vcc, exec, s[40:41]
	v_cvt_pk_bf16_f32 v24, v28, v29
	v_cvt_pk_bf16_f32 v25, v30, v31
	s_mov_b64 s[2:3], -1
	ds_write_b64 v234, v[24:25] offset:32
	s_cbranch_vccnz .LBB0_846
	v_mov_b32_e32 v24, v164
	v_mov_b32_e32 v25, v165
	v_mov_b32_e32 v26, v166
	v_mov_b32_e32 v27, v167
	s_mov_b64 s[2:3], 0

; __device__ __forceinline__ unsigned cvt_pk_bf16(float lo, float hi) { unsigned r; asm volatile("v_cvt_pk_bf16_f32 %0, %1, %2" : "=v"(r) : "v"(lo), "v"(hi)); return r; }
;     __device__ __forceinline__ void operator()(const f32x4 (&acc)[2][2][4][2], const Unit& u, int wr, int wc, int fr, int fq) const {
;     ...
;                     for (int n = 0; n < 2; ++n) { f32x4 r;
;                         if (R32) r = *(const f32x4*)(R32 + ro + bj * HALF + n * 16);
;                         else { typedef unsigned u32x2_t __attribute__((ext_vector_type(2))); const u32x2_t rw = *(const u32x2_t*)(R16 + ro + bj * HALF + n * 16); const unsigned r0 = rw.x, r1 = rw.y;
;                             r = (f32x4){__builtin_bit_cast(float, r0 << 16), __builtin_bit_cast(float, r0 & 0xffff0000u), __builtin_bit_cast(float, r1 << 16), __builtin_bit_cast(float, r1 & 0xffff0000u)}; }
;                         const f32x4 v = acc[ai][bj][m][n] + r;
;                         typedef unsigned u32x2_s __attribute__((ext_vector_type(2))); u32x2_s w; w.x = cvt_pk_bf16(v[0], v[1]); w.y = cvt_pk_bf16(v[2], v[3]);
;                         *(u32x2_s*)(XB + ro + bj * HALF + n * 16) = w;
.LBB0_848:
	v_pk_add_f32 v[26:27], v[22:23], v[26:27]
	v_pk_add_f32 v[24:25], v[20:21], v[24:25]
	s_and_b64 vcc, exec, s[40:41]
	v_cvt_pk_bf16_f32 v20, v24, v25
	v_cvt_pk_bf16_f32 v21, v26, v27
	s_mov_b64 s[2:3], -1
	ds_write_b64 v234, v[20:21] offset:64
	s_cbranch_vccnz .LBB0_850
	v_mov_b32_e32 v20, v168
	v_mov_b32_e32 v21, v169
	v_mov_b32_e32 v22, v170
	v_mov_b32_e32 v23, v171
	s_mov_b64 s[2:3], 0

; __device__ __forceinline__ unsigned cvt_pk_bf16(float lo, float hi) { unsigned r; asm volatile("v_cvt_pk_bf16_f32 %0, %1, %2" : "=v"(r) : "v"(lo), "v"(hi)); return r; }
;     __device__ __forceinline__ void operator()(const f32x4 (&acc)[2][2][4][2], const Unit& u, int wr, int wc, int fr, int fq) const {
;     ...
;             for (int m = 0; m < 4; ++m) { const int row = row0 + ai * HALF + m * 16; const size_t ro = (size_t)row * 2048 + col0;
;                 float s = 0.f;
; #pragma unroll
;                 for (int bj = 0; bj < 2; ++bj)
; #pragma unroll
;                     for (int n = 0; n < 2; ++n) { f32x4 r;
;                         if (R32) r = *(const f32x4*)(R32 + ro + bj * HALF + n * 16);
;                         else { typedef unsigned u32x2_t __attribute__((ext_vector_type(2))); const u32x2_t rw = *(const u32x2_t*)(R16 + ro + bj * HALF + n * 16); const unsigned r0 = rw.x, r1 = rw.y;
;                             r = (f32x4){__builtin_bit_cast(float, r0 << 16), __builtin_bit_cast(float, r0 & 0xffff0000u), __builtin_bit_cast(float, r1 << 16), __builtin_bit_cast(float, r1 & 0xffff0000u)}; }
;                         const f32x4 v = acc[ai][bj][m][n] + r;
;                         typedef unsigned u32x2_s __attribute__((ext_vector_type(2))); u32x2_s w; w.x = cvt_pk_bf16(v[0], v[1]); w.y = cvt_pk_bf16(v[2], v[3]);
;                         *(u32x2_s*)(XB + ro + bj * HALF + n * 16) = w;
.LBB0_854:
	s_or_b64 exec, exec, s[2:3]
	s_mov_b64 s[2:3], 0x58000
	v_readlane_b32 s4, v252, 2
	v_lshl_add_u64 v[26:27], v[140:141], 0, s[2:3]
	v_readlane_b32 s5, v252, 3
	s_mov_b64 s[2:3], -1
	s_and_b64 vcc, exec, s[40:41]
	v_lshl_add_u64 v[22:23], v[26:27], 2, s[4:5]
	v_readlane_b32 s6, v252, 4
	v_readlane_b32 s7, v252, 5
	v_readlane_b32 s8, v252, 6
	v_readlane_b32 s9, v252, 7
	v_readlane_b32 s10, v252, 8
	v_readlane_b32 s11, v252, 9
	v_readlane_b32 s12, v252, 10
	v_readlane_b32 s13, v252, 11
	v_readlane_b32 s14, v252, 12
	v_readlane_b32 s15, v252, 13
	v_readlane_b32 s16, v252, 14
	v_readlane_b32 s17, v252, 15
	v_readlane_b32 s18, v252, 16
	v_readlane_b32 s19, v252, 17
	s_cbranch_vccnz .LBB0_856
	s_waitcnt lgkmcnt(0)
	global_load_dwordx4 v[156:159], v[22:23], off
	global_load_dwordx4 v[160:163], v[22:23], off offset:64
	global_load_dwordx4 v[164:167], v[22:23], off offset:512
	global_load_dwordx4 v[168:171], v[22:23], off offset:576
	s_waitcnt vmcnt(0)
	v_mov_b32_e32 v16, v156
	v_mov_b32_e32 v17, v157
	v_mov_b32_e32 v18, v158
	v_mov_b32_e32 v19, v159
	s_mov_b64 s[2:3], 0

; __device__ __forceinline__ unsigned cvt_pk_bf16(float lo, float hi) { unsigned r; asm volatile("v_cvt_pk_bf16_f32 %0, %1, %2" : "=v"(r) : "v"(lo), "v"(hi)); return r; }
;     __device__ __forceinline__ void operator()(const f32x4 (&acc)[2][2][4][2], const Unit& u, int wr, int wc, int fr, int fq) const {
;     ...
;                     for (int n = 0; n < 2; ++n) { f32x4 r;
;                         if (R32) r = *(const f32x4*)(R32 + ro + bj * HALF + n * 16);
;                         else { typedef unsigned u32x2_t __attribute__((ext_vector_type(2))); const u32x2_t rw = *(const u32x2_t*)(R16 + ro + bj * HALF + n * 16); const unsigned r0 = rw.x, r1 = rw.y;
;                             r = (f32x4){__builtin_bit_cast(float, r0 << 16), __builtin_bit_cast(float, r0 & 0xffff0000u), __builtin_bit_cast(float, r1 << 16), __builtin_bit_cast(float, r1 & 0xffff0000u)}; }
;                         const f32x4 v = acc[ai][bj][m][n] + r;
;                         typedef unsigned u32x2_s __attribute__((ext_vector_type(2))); u32x2_s w; w.x = cvt_pk_bf16(v[0], v[1]); w.y = cvt_pk_bf16(v[2], v[3]);
;                         *(u32x2_s*)(XB + ro + bj * HALF + n * 16) = w;
.LBB0_858:
	v_pk_add_f32 v[18:19], v[14:15], v[18:19]
	s_waitcnt lgkmcnt(0)
	v_pk_add_f32 v[24:25], v[12:13], v[16:17]
	v_lshl_add_u64 v[16:17], v[26:27], 1, s[90:91]
	v_cvt_pk_bf16_f32 v12, v24, v25
	v_cvt_pk_bf16_f32 v13, v18, v19
	s_and_b64 vcc, exec, s[40:41]
	s_mov_b64 s[2:3], -1
	ds_write_b64 v234, v[12:13]
	s_cbranch_vccnz .LBB0_860
	v_mov_b32_e32 v12, v160
	v_mov_b32_e32 v13, v161
	v_mov_b32_e32 v14, v162
	v_mov_b32_e32 v15, v163
	s_mov_b64 s[2:3], 0

; __device__ __forceinline__ unsigned cvt_pk_bf16(float lo, float hi) { unsigned r; asm volatile("v_cvt_pk_bf16_f32 %0, %1, %2" : "=v"(r) : "v"(lo), "v"(hi)); return r; }
;     __device__ __forceinline__ void operator()(const f32x4 (&acc)[2][2][4][2], const Unit& u, int wr, int wc, int fr, int fq) const {
;     ...
;                     for (int n = 0; n < 2; ++n) { f32x4 r;
;                         if (R32) r = *(const f32x4*)(R32 + ro + bj * HALF + n * 16);
;                         else { typedef unsigned u32x2_t __attribute__((ext_vector_type(2))); const u32x2_t rw = *(const u32x2_t*)(R16 + ro + bj * HALF + n * 16); const unsigned r0 = rw.x, r1 = rw.y;
;                             r = (f32x4){__builtin_bit_cast(float, r0 << 16), __builtin_bit_cast(float, r0 & 0xffff0000u), __builtin_bit_cast(float, r1 << 16), __builtin_bit_cast(float, r1 & 0xffff0000u)}; }
;                         const f32x4 v = acc[ai][bj][m][n] + r;
;                         typedef unsigned u32x2_s __attribute__((ext_vector_type(2))); u32x2_s w; w.x = cvt_pk_bf16(v[0], v[1]); w.y = cvt_pk_bf16(v[2], v[3]);
;                         *(u32x2_s*)(XB + ro + bj * HALF + n * 16) = w;
.LBB0_862:
	v_pk_add_f32 v[14:15], v[10:11], v[14:15]
	v_pk_add_f32 v[12:13], v[8:9], v[12:13]
	s_and_b64 vcc, exec, s[40:41]
	v_cvt_pk_bf16_f32 v8, v12, v13
	v_cvt_pk_bf16_f32 v9, v14, v15
	s_mov_b64 s[2:3], -1
	ds_write_b64 v234, v[8:9] offset:32
	s_cbranch_vccnz .LBB0_864
	v_mov_b32_e32 v8, v164
	v_mov_b32_e32 v9, v165
	v_mov_b32_e32 v10, v166
	v_mov_b32_e32 v11, v167
	s_mov_b64 s[2:3], 0

; __device__ __forceinline__ unsigned cvt_pk_bf16(float lo, float hi) { unsigned r; asm volatile("v_cvt_pk_bf16_f32 %0, %1, %2" : "=v"(r) : "v"(lo), "v"(hi)); return r; }
;     __device__ __forceinline__ void operator()(const f32x4 (&acc)[2][2][4][2], const Unit& u, int wr, int wc, int fr, int fq) const {
;     ...
;                     for (int n = 0; n < 2; ++n) { f32x4 r;
;                         if (R32) r = *(const f32x4*)(R32 + ro + bj * HALF + n * 16);
;                         else { typedef unsigned u32x2_t __attribute__((ext_vector_type(2))); const u32x2_t rw = *(const u32x2_t*)(R16 + ro + bj * HALF + n * 16); const unsigned r0 = rw.x, r1 = rw.y;
;                             r = (f32x4){__builtin_bit_cast(float, r0 << 16), __builtin_bit_cast(float, r0 & 0xffff0000u), __builtin_bit_cast(float, r1 << 16), __builtin_bit_cast(float, r1 & 0xffff0000u)}; }
;                         const f32x4 v = acc[ai][bj][m][n] + r;
;                         typedef unsigned u32x2_s __attribute__((ext_vector_type(2))); u32x2_s w; w.x = cvt_pk_bf16(v[0], v[1]); w.y = cvt_pk_bf16(v[2], v[3]);
;                         *(u32x2_s*)(XB + ro + bj * HALF + n * 16) = w;
.LBB0_866:
	v_pk_add_f32 v[10:11], v[6:7], v[10:11]
	v_pk_add_f32 v[8:9], v[4:5], v[8:9]
	s_and_b64 vcc, exec, s[40:41]
	v_cvt_pk_bf16_f32 v4, v8, v9
	v_cvt_pk_bf16_f32 v5, v10, v11
	s_mov_b64 s[2:3], -1
	ds_write_b64 v234, v[4:5] offset:64
	s_cbranch_vccnz .LBB0_868
	v_mov_b32_e32 v4, v168
	v_mov_b32_e32 v5, v169
	v_mov_b32_e32 v6, v170
	v_mov_b32_e32 v7, v171
	s_mov_b64 s[2:3], 0
